# speedup vs baseline: 1.0225x; 1.0225x over previous
.Lp1_fin:
	s_lshl_b64 s[0:1], s[20:21], 1
	s_add_u32 s0, s18, s0
	s_addc_u32 s1, s19, s1
	global_load_dwordx4 v[2:5], v[66:67], off
	global_load_dwordx4 v[6:9], v[68:69], off
	v_lshlrev_b32_e32 v10, 1, v79
	global_load_dwordx4 v[10:13], v10, s[0:1]
	v_lshlrev_b32_e32 v14, 1, v80
	global_load_dwordx4 v[14:17], v14, s[0:1]
	v_mov_b32_e32 v200, 0
	v_mov_b32_e32 v201, 0
	v_mov_b32_e32 v202, 0
	v_mov_b32_e32 v83, 0
	v_exp_f32_e32 v34, v34
	v_exp_f32_e32 v35, v35
	v_add_f32_e32 v200, v200, v34
	v_exp_f32_e32 v36, v36
	v_add_f32_e32 v201, v201, v35
	v_exp_f32_e32 v37, v37
	v_add_f32_e32 v202, v202, v36
	v_exp_f32_e32 v38, v38
	v_add_f32_e32 v83, v83, v37
	v_exp_f32_e32 v39, v39
	v_add_f32_e32 v200, v200, v38
	v_exp_f32_e32 v40, v40
	v_add_f32_e32 v201, v201, v39
	v_exp_f32_e32 v41, v41
	v_add_f32_e32 v202, v202, v40
	v_exp_f32_e32 v42, v42
	v_add_f32_e32 v83, v83, v41
	v_exp_f32_e32 v43, v43
	v_add_f32_e32 v200, v200, v42
	v_exp_f32_e32 v44, v44
	v_add_f32_e32 v201, v201, v43
	v_exp_f32_e32 v45, v45
	v_add_f32_e32 v202, v202, v44
	v_exp_f32_e32 v46, v46
	v_add_f32_e32 v83, v83, v45
	v_exp_f32_e32 v47, v47
	v_add_f32_e32 v200, v200, v46
	v_exp_f32_e32 v48, v48
	v_add_f32_e32 v201, v201, v47
	v_exp_f32_e32 v49, v49
	v_add_f32_e32 v202, v202, v48
	v_exp_f32_e32 v50, v50
	v_add_f32_e32 v83, v83, v49
	v_exp_f32_e32 v51, v51
	v_add_f32_e32 v200, v200, v50
	v_exp_f32_e32 v52, v52
	v_add_f32_e32 v201, v201, v51
	v_exp_f32_e32 v53, v53
	v_add_f32_e32 v202, v202, v52
	v_exp_f32_e32 v54, v54
	v_add_f32_e32 v83, v83, v53
	v_exp_f32_e32 v55, v55
	v_add_f32_e32 v200, v200, v54
	v_exp_f32_e32 v56, v56
	v_add_f32_e32 v201, v201, v55
	v_exp_f32_e32 v57, v57
	v_add_f32_e32 v202, v202, v56
	v_exp_f32_e32 v58, v58
	v_add_f32_e32 v83, v83, v57
	v_exp_f32_e32 v59, v59
	v_add_f32_e32 v200, v200, v58
	v_exp_f32_e32 v60, v60
	v_add_f32_e32 v201, v201, v59
	v_exp_f32_e32 v61, v61
	v_add_f32_e32 v202, v202, v60
	v_exp_f32_e32 v62, v62
	v_add_f32_e32 v83, v83, v61
	v_exp_f32_e32 v63, v63
	v_add_f32_e32 v200, v200, v62
	v_exp_f32_e32 v64, v64
	v_add_f32_e32 v201, v201, v63
	v_exp_f32_e32 v65, v65
	v_add_f32_e32 v202, v202, v64
	v_add_f32_e32 v83, v83, v65
	v_add_f32_e32 v200, v200, v201
	v_add_f32_e32 v202, v202, v83
	v_add_f32_e32 v200, v200, v202
	v_add_f32_e32 v82, v82, v200
	s_barrier
	v_mbcnt_lo_u32_b32 v21, -1, 0
	v_mbcnt_hi_u32_b32 v21, -1, v21
	v_and_b32_e32 v23, 64, v21
	v_xor_b32_e32 v22, 32, v21
	v_add_u32_e32 v24, 64, v23
	v_cmp_lt_i32_e32 vcc, v22, v24
	v_cndmask_b32_e32 v21, v21, v22, vcc
	v_lshlrev_b32_e32 v21, 2, v21
	ds_bpermute_b32 v22, v21, v81
	v_mov_b32_e32 v18, v82
	ds_bpermute_b32 v19, v21, v18
	v_max_f32_e32 v21, v81, v81
	s_mov_b32 s15, 0
	s_waitcnt lgkmcnt(1)
	v_max_f32_e32 v20, v22, v22
	v_max_f32_e32 v20, v21, v20
	v_sub_f32_e32 v22, v22, v20
	v_sub_f32_e32 v21, v81, v20
	v_exp_f32_e32 v22, v22
	v_exp_f32_e32 v21, v21
	s_lshl_b64 s[18:19], s[14:15], 18
	v_mov_b32_e32 v131, 0
	s_waitcnt lgkmcnt(0)
	v_mul_f32_e32 v19, v22, v19
	v_fmac_f32_e32 v19, v18, v21
	v_div_scale_f32 v18, s[10:11], v19, v19, 1.0
	s_movk_i32 s10, 0x60
	s_nop 0
	v_mad_u32_u24 v188, v73, s10, v74
	v_mad_u32_u24 v189, v75, s10, v74
	s_waitcnt vmcnt(3)
	ds_write_b128 v77, v[2:5]
	s_waitcnt vmcnt(2)
	ds_write_b128 v78, v[6:9]
	v_lshlrev_b32_e32 v2, 1, v188
	s_waitcnt vmcnt(1)
	ds_write_b128 v2, v[10:13]
	v_lshlrev_b32_e32 v2, 1, v189
	s_mul_i32 s10, s14, 0x1200
	s_waitcnt vmcnt(0)
	ds_write_b128 v2, v[14:17]
	s_add_i32 s10, s10, 0xa800
	v_lshrrev_b32_e32 v2, 2, v0
	v_and_or_b32 v3, v2, 3, v1
	s_movk_i32 s11, 0x48
	v_mov_b32_e32 v5, s10
	v_add_u32_e32 v4, s10, v76
	v_mad_u32_u24 v5, v3, s11, v5
	s_lshl_b64 s[10:11], s[12:13], 24
	s_and_b32 s13, s2, 15
	s_lshl_b32 s13, s13, 20
	v_and_b32_e32 v0, 3, v0
	s_or_b32 s10, s10, s13
	v_and_or_b32 v0, v2, 4, v0
	s_add_u32 s10, s10, s18
	v_lshlrev_b32_e32 v0, 3, v0
	v_mul_u32_u24_e32 v2, 0xc0, v3
	v_lshlrev_b32_e32 v3, 13, v72
	s_addc_u32 s11, s11, s19
	v_or_b32_e32 v185, v2, v0
	v_or_b32_e32 v2, v3, v164
	s_add_u32 s10, s4, s10
	v_lshlrev_b32_e32 v130, 2, v2
	s_addc_u32 s11, s5, s11
	v_rcp_f32_e32 v21, v18
	s_nop 0
	v_fma_f32 v22, -v18, v21, 1.0
	v_fmac_f32_e32 v21, v22, v21
	v_div_scale_f32 v22, vcc, 1.0, v19, 1.0
	v_mul_f32_e32 v24, v22, v21
	v_fma_f32 v25, -v18, v24, v22
	v_fmac_f32_e32 v24, v25, v21
	v_fma_f32 v18, -v18, v24, v22
	v_div_fmas_f32 v18, v18, v21, v24
	v_lshlrev_b32_e32 v184, 2, v72
	v_div_fixup_f32 v18, v18, v19, 1.0
	v_or_b32_e32 v19, v184, v23
	v_lshlrev_b32_e32 v19, 2, v19
	ds_bpermute_b32 v33, v19, v20 offset:36
	ds_bpermute_b32 v32, v19, v20 offset:40
	ds_bpermute_b32 v35, v19, v20 offset:44
	ds_bpermute_b32 v34, v19, v20 offset:64
	ds_bpermute_b32 v37, v19, v20 offset:68
	ds_bpermute_b32 v36, v19, v20 offset:72
	ds_bpermute_b32 v39, v19, v20 offset:76
	ds_bpermute_b32 v38, v19, v20 offset:96
	ds_bpermute_b32 v41, v19, v20 offset:100
	ds_bpermute_b32 v40, v19, v20 offset:104
	ds_bpermute_b32 v43, v19, v20 offset:108
	ds_bpermute_b32 v46, v19, v20 offset:32
	ds_bpermute_b32 v47, v19, v20 offset:12
	ds_bpermute_b32 v42, v19, v20 offset:8
	ds_bpermute_b32 v45, v19, v20 offset:4
	ds_bpermute_b32 v44, v19, v20
	ds_bpermute_b32 v183, v19, v18
	ds_bpermute_b32 v182, v19, v18 offset:4
	ds_bpermute_b32 v181, v19, v18 offset:8
	ds_bpermute_b32 v180, v19, v18 offset:12
	ds_bpermute_b32 v179, v19, v18 offset:32
	ds_bpermute_b32 v178, v19, v18 offset:36
	ds_bpermute_b32 v177, v19, v18 offset:40
	ds_bpermute_b32 v176, v19, v18 offset:44
	ds_bpermute_b32 v175, v19, v18 offset:64
	ds_bpermute_b32 v174, v19, v18 offset:68
	ds_bpermute_b32 v173, v19, v18 offset:72
	ds_bpermute_b32 v172, v19, v18 offset:76
	ds_bpermute_b32 v171, v19, v18 offset:96
	ds_bpermute_b32 v170, v19, v18 offset:100
	ds_bpermute_b32 v169, v19, v18 offset:104
	ds_bpermute_b32 v168, v19, v18 offset:108
	v_mov_b32_e32 v3, v131
	v_add_u32_e32 v187, v4, v1
	s_mov_b64 s[42:43], s[10:11]
	s_mov_b64 s[10:11], 0
	s_movk_i32 s13, 0x3000
	s_waitcnt lgkmcnt(14)
	v_xor_b32_e32 v63, 0x80000000, v43
	v_xor_b32_e32 v62, 0x80000000, v40
	v_xor_b32_e32 v61, 0x80000000, v41
	v_xor_b32_e32 v60, 0x80000000, v38
	v_xor_b32_e32 v59, 0x80000000, v39
	v_xor_b32_e32 v58, 0x80000000, v36
	v_xor_b32_e32 v57, 0x80000000, v37
	v_xor_b32_e32 v56, 0x80000000, v34
	v_xor_b32_e32 v55, 0x80000000, v35
	v_xor_b32_e32 v54, 0x80000000, v32
	v_xor_b32_e32 v53, 0x80000000, v33
	v_add_u32_e32 v186, v5, v0
	v_xor_b32_e32 v52, 0x80000000, v46
	v_xor_b32_e32 v51, 0x80000000, v47
	v_xor_b32_e32 v50, 0x80000000, v42
	v_xor_b32_e32 v49, 0x80000000, v45
	v_xor_b32_e32 v48, 0x80000000, v44
	v_mov_b32_e32 v0, v131
	v_mov_b32_e32 v1, v131
	v_mov_b32_e32 v2, v131
	v_mov_b32_e32 v4, v131
	v_mov_b32_e32 v5, v131
	v_mov_b32_e32 v6, v131
	v_mov_b32_e32 v7, v131
	v_mov_b32_e32 v8, v131
	v_mov_b32_e32 v9, v131
	v_mov_b32_e32 v10, v131
	v_mov_b32_e32 v11, v131
	v_mov_b32_e32 v12, v131
	v_mov_b32_e32 v13, v131
	v_mov_b32_e32 v14, v131
	v_mov_b32_e32 v15, v131
	v_mov_b32_e32 v16, v131
	v_mov_b32_e32 v17, v131
	v_mov_b32_e32 v18, v131
	v_mov_b32_e32 v19, v131
	v_mov_b32_e32 v20, v131
	v_mov_b32_e32 v21, v131
	v_mov_b32_e32 v22, v131
	v_mov_b32_e32 v23, v131
	v_mov_b32_e32 v24, v131
	v_mov_b32_e32 v25, v131
	v_mov_b32_e32 v26, v131
	v_mov_b32_e32 v27, v131
	v_mov_b32_e32 v28, v131
	v_mov_b32_e32 v29, v131
	v_mov_b32_e32 v30, v131
	v_mov_b32_e32 v31, v131
	v_add_u32_e32 v131, 0x800, v187
	v_or_b32_e32 v132, 0x80, v130
	v_or_b32_e32 v136, 0x2080, v130
	v_or_b32_e32 v140, 0x4080, v130
	v_or_b32_e32 v144, 0x6080, v130
	v_or_b32_e32 v148, 0x10080, v130
	v_or_b32_e32 v152, 0x12080, v130
	v_or_b32_e32 v156, 0x14080, v130
	v_or_b32_e32 v160, 0x16080, v130
	v_or_b32_e32 v162, 0x20000, v130
	v_or_b32_e32 v158, 0x22000, v130
	v_or_b32_e32 v154, 0x24000, v130
	v_or_b32_e32 v150, 0x26000, v130
	v_or_b32_e32 v146, 0x30000, v130
	v_or_b32_e32 v142, 0x32000, v130
	v_or_b32_e32 v138, 0x34000, v130
	v_or_b32_e32 v134, 0x36000, v130
	s_add_u32 s8, s8, 0x2000
	s_addc_u32 s9, s9, 0
	s_add_u32 s0, s0, 0x2000
	s_addc_u32 s1, s1, 0
	v_add_u32_e32 v204, 0x1000, v128
	s_waitcnt lgkmcnt(0)
	s_barrier
